# GLA prep loads use SGPR base + 32-bit VGPR offset (drops 75 64-bit VALU address adds per chunk pair)
# baseline (speedup 1.0000x reference)
; __device__ __forceinline__ void gla_fast_unit(int unit, const bf16_t* P, const float* w_up, const float* b_up, float* Of, float* Ob, LAS unsigned char* lds0) {
;     ...
;         bf16x8 wfr[4]; float bu[4];
; #pragma unroll
;         for (int it = 0; it < 4; ++it) { unsigned w[4] = {0u, 0u, 0u, 0u};
;             if (q < 2) {
; #pragma unroll
;                 for (int j = 0; j < 4; ++j) w[j] = pk2(w_up[(size_t)(dir * 16 + 8 * q + 2 * j) * 512 + h * 64 + 16 * it + l15], w_up[(size_t)(dir * 16 + 8 * q + 2 * j + 1) * 512 + h * 64 + 16 * it + l15]); }
;             wfr[it] = __builtin_bit_cast(bf16x8, (u32x4){w[0], w[1], w[2], w[3]}); bu[it] = b_up[dir * 512 + h * 64 + 16 * it + l15]; }
;         u32x4 graw0; unsigned short qr0[4][4], kr0[4][4]; u32x4 vraw0[4];
;         const unsigned goff = (unsigned)((dir ? 63 - (16 * pw + l15) : 16 * pw + l15) * (LDP1 * 2) + (6144 + dir * 16 + 8 * q) * 2);
;         unsigned qkoff[4], voff[4];
; #pragma unroll
;         for (int r = 0; r < 4; ++r) { const int p = 16 * pw + 4 * q + r; qkoff[r] = (unsigned)((dir ? 63 - p : p) * (LDP1 * 2) + (h * 64 + l15) * 2); }
; #pragma unroll
;         for (int i = 0; i < 4; ++i) { const int piece = ptid + 256 * i, p = piece >> 4, ch = piece & 15; voff[i] = (unsigned)((dir ? 63 - p : p) * (LDP1 * 2) + (5120 + h * 128 + 8 * ch) * 2); }
;     ...
;         GLA_LOAD(0, graw0, qr0, kr0, vraw0);
.LBB0_1140:
	s_or_b64 exec, exec, s[2:3]
	global_load_dword v30, v[16:17], off offset:192
	s_add_i32 s12, s34, -4
	s_lshl_b32 s35, s9, 8
	s_addk_i32 s35, 0x4000
	s_lshl_b32 s13, s12, 4
	v_xor_b32_e32 v11, 63, v1
	s_and_b64 s[2:3], s[4:5], exec
	v_or_b32_e32 v13, s13, v1
	v_subrev_u32_e32 v11, s13, v11
	s_cselect_b32 s2, 0, 0xc0
	v_cndmask_b32_e64 v11, v11, v13, s[4:5]
	s_movk_i32 s11, 0x3200
	s_or_b32 s2, s2, s35
	v_mov_b32_e32 v34, 0
	v_lshl_add_u32 v12, s8, 5, v176
	v_mul_lo_u32 v11, v11, s11
	s_mul_hi_i32 s3, s2, 0x3200
	s_mulk_i32 s2, 0x3200
	v_readlane_b32 s8, v254, 61
	v_mov_b32_e32 v36, v34
	v_mov_b32_e32 v37, v34
	v_or_b32_e32 v11, v11, v12
	v_readlane_b32 s9, v254, 62
	s_add_u32 s2, s8, s2
	v_mov_b32_e32 v35, v34
	v_mov_b64_e32 v[38:39], v[36:37]
	v_add_u32_e32 v56, 0x3000, v11
	s_addc_u32 s3, s9, s3
	v_mov_b32_e32 v57, v34
	v_mov_b64_e32 v[36:37], v[34:35]
	s_and_saveexec_b64 s[8:9], s[6:7]
	s_cbranch_execz .LBB0_1142
	global_load_dwordx4 v[36:39], v56, s[2:3]

.LBB0_1143:
	s_or_b64 exec, exec, s[28:29]
	global_load_ushort v35, v66, s[2:3]
	global_load_ushort v190, v68, s[2:3]
	global_load_ushort v191, v70, s[2:3]
	global_load_ushort v192, v72, s[2:3]
	global_load_ushort v193, v74, s[2:3]
	global_load_ushort v194, v76, s[2:3]
	global_load_ushort v195, v78, s[2:3]
	global_load_ushort v196, v80, s[2:3]
	global_load_ushort v214, v82, s[2:3]
	global_load_ushort v215, v84, s[2:3]
	global_load_ushort v216, v88, s[2:3]
	global_load_ushort v217, v90, s[2:3]
	global_load_ushort v218, v92, s[2:3]
	global_load_ushort v219, v94, s[2:3]
	global_load_ushort v220, v96, s[2:3]
	global_load_ushort v221, v98, s[2:3]
	global_load_ushort v222, v100, s[2:3]
	global_load_ushort v223, v102, s[2:3]
	global_load_ushort v224, v104, s[2:3]
	global_load_ushort v225, v106, s[2:3]
	global_load_ushort v226, v108, s[2:3]
	global_load_ushort v227, v110, s[2:3]
	global_load_ushort v229, v112, s[2:3]
	global_load_ushort v230, v114, s[2:3]
	global_load_ushort v231, v116, s[2:3]
	global_load_ushort v232, v118, s[2:3]
	global_load_ushort v233, v120, s[2:3]
	global_load_ushort v234, v122, s[2:3]
	global_load_ushort v235, v124, s[2:3]
	global_load_ushort v236, v126, s[2:3]
	global_load_ushort v237, v128, s[2:3]
	global_load_ushort v238, v130, s[2:3]
	global_load_dwordx4 v[40:43], v58, s[2:3]
	s_nop 0
	global_load_dwordx4 v[44:47], v60, s[2:3]
	s_nop 0
	global_load_dwordx4 v[48:51], v62, s[2:3]
	s_nop 0
	global_load_dwordx4 v[52:55], v64, s[2:3]

.LBB0_1169:
	s_mul_hi_i32 s3, s29, 0x3200
	s_mul_i32 s2, s29, 0x3200
	v_readlane_b32 s28, v254, 61
	v_mov_b32_e32 v36, v34
	v_mov_b32_e32 v37, v34
	v_readlane_b32 s29, v254, 62
	s_add_u32 s2, s28, s2
	v_mov_b32_e32 v35, v34
	v_mov_b64_e32 v[38:39], v[36:37]
	s_addc_u32 s3, s29, s3
	v_mov_b64_e32 v[36:37], v[34:35]
	s_and_saveexec_b64 s[28:29], s[6:7]
	s_cbranch_execz .LBB0_1171
	global_load_dwordx4 v[36:39], v56, s[2:3]

.LBB0_1196:
	s_mul_hi_i32 s3, s28, 0x3200
	s_mul_i32 s2, s28, 0x3200
	v_readlane_b32 s28, v254, 61
	v_mov_b32_e32 v36, v34
	v_mov_b32_e32 v37, v34
	v_readlane_b32 s29, v254, 62
	s_add_u32 s2, s28, s2
	v_mov_b32_e32 v35, v34
	v_mov_b64_e32 v[38:39], v[36:37]
	s_addc_u32 s3, s29, s3
	v_mov_b64_e32 v[36:37], v[34:35]
	s_and_saveexec_b64 s[28:29], s[6:7]
	s_cbranch_execz .LBB0_1143
	global_load_dwordx4 v[36:39], v56, s[2:3]
	s_branch .LBB0_1143
